# L1 rwkv yfin epilogue: row loads of token row q+1 issued during row q (one row ahead) into spare VGPRs, params before the prefetch
# baseline (speedup 1.0000x reference)
.LBB0_3735:
	s_ashr_i32 s0, s8, 31
	s_lshr_b32 s0, s0, 25
	s_add_i32 s16, s8, s0
	s_and_b32 s3, s16, 0xffffff80
	s_ashr_i32 s0, s16, 10
	s_add_i32 s6, s8, s3
	s_ashr_i32 s1, s0, 31
	s_ashr_i32 s7, s6, 31
	s_add_i32 s10, s6, 0x80
	s_lshl_b64 s[12:13], s[0:1], 12
	s_lshl_b64 s[0:1], s[6:7], 13
	s_lshl_b64 s[6:7], s[6:7], 12
	v_lshl_add_u64 v[4:5], v[128:129], 0, s[6:7]
	global_load_dwordx4 v[46:49], v[4:5], off
	global_load_dwordx4 v[18:21], v[4:5], off offset:1024
	v_lshl_add_u64 v[6:7], v[132:133], 0, s[6:7]
	s_ashr_i32 s11, s10, 31
	v_lshl_add_u64 v[2:3], v[114:115], 0, s[0:1]
	global_load_dwordx2 v[150:151], v[6:7], off
	global_load_dwordx2 v[148:149], v[6:7], off offset:512
	global_load_dwordx2 v[146:147], v[6:7], off offset:1024
	global_load_dwordx2 v[144:145], v[6:7], off offset:1536
	global_load_dwordx4 v[42:45], v[4:5], off offset:2048
	global_load_dwordx4 v[14:17], v[4:5], off offset:3072
	global_load_dwordx2 v[142:143], v[6:7], off offset:2048
	global_load_dwordx2 v[140:141], v[6:7], off offset:2560
	global_load_dwordx2 v[138:139], v[6:7], off offset:3072
	global_load_dwordx2 v[136:137], v[6:7], off offset:3584
	s_lshl_b64 s[0:1], s[10:11], 12
	v_readfirstlane_b32 s14, v2
	v_readfirstlane_b32 s15, v3
	v_lshl_add_u64 v[4:5], v[130:131], 0, s[0:1]
	s_nop 3
	global_load_dwordx2 v[62:63], v125, s[14:15]
	global_load_dwordx2 v[64:65], v125, s[14:15] offset:512
	global_load_dwordx2 v[38:39], v125, s[14:15] offset:1024
	global_load_dwordx2 v[40:41], v125, s[14:15] offset:1536
	global_load_dwordx2 v[58:59], v125, s[14:15] offset:2048
	global_load_dwordx2 v[60:61], v125, s[14:15] offset:2560
	global_load_dwordx2 v[34:35], v125, s[14:15] offset:3072
	global_load_dwordx2 v[36:37], v125, s[14:15] offset:3584
	global_load_dwordx2 v[54:55], v127, s[14:15]
	global_load_dwordx2 v[56:57], v127, s[14:15] offset:512
	global_load_dwordx2 v[30:31], v178, s[14:15]
	global_load_dwordx2 v[32:33], v178, s[14:15] offset:512
	global_load_dwordx2 v[50:51], v123, s[14:15]
	global_load_dwordx2 v[52:53], v123, s[14:15] offset:512
	global_load_dwordx2 v[26:27], v179, s[14:15]
	global_load_dwordx2 v[28:29], v179, s[14:15] offset:512
	global_load_dwordx4 v[22:25], v[4:5], off offset:2048
	global_load_dwordx4 v[6:9], v[4:5], off offset:3072
	s_lshl_b64 s[6:7], s[10:11], 13
	v_lshl_add_u64 v[66:67], v[112:113], 0, s[0:1]
	v_lshl_add_u64 v[2:3], v[114:115], 0, s[6:7]
	v_lshl_add_u64 v[152:153], v[134:135], 1, v[66:67]
	v_readfirstlane_b32 s0, v2
	v_readfirstlane_b32 s1, v3
	global_load_dwordx4 v[10:13], v[4:5], off
	s_nop 0
	global_load_dwordx4 v[2:5], v[4:5], off offset:1024
	v_readfirstlane_b32 s6, v66
	v_readfirstlane_b32 s7, v67
	global_load_dwordx2 v[168:169], v[152:153], off offset:2048
	global_load_dwordx2 v[94:95], v125, s[0:1]
	global_load_dwordx2 v[96:97], v125, s[0:1] offset:512
	global_load_dwordx2 v[78:79], v125, s[0:1] offset:1024
	global_load_dwordx2 v[80:81], v125, s[0:1] offset:1536
	global_load_dwordx2 v[90:91], v125, s[0:1] offset:2048
	global_load_dwordx2 v[92:93], v125, s[0:1] offset:2560
	global_load_dwordx2 v[74:75], v125, s[0:1] offset:3072
	global_load_dwordx2 v[76:77], v125, s[0:1] offset:3584
	global_load_dwordx2 v[86:87], v127, s[0:1]
	global_load_dwordx2 v[88:89], v127, s[0:1] offset:512
	global_load_dwordx2 v[70:71], v178, s[0:1]
	global_load_dwordx2 v[72:73], v178, s[0:1] offset:512
	global_load_dwordx2 v[82:83], v123, s[0:1]
	global_load_dwordx2 v[84:85], v123, s[0:1] offset:512
	global_load_dwordx2 v[66:67], v179, s[0:1]
	global_load_dwordx2 v[68:69], v179, s[0:1] offset:512
	global_load_dwordx2 v[174:175], v[152:153], off offset:2560
	global_load_dwordx2 v[172:173], v[152:153], off offset:3072
	global_load_dwordx2 v[170:171], v[152:153], off offset:3584
	global_load_dwordx2 v[166:167], v180, s[6:7]
	global_load_dwordx2 v[164:165], v[152:153], off offset:512
	global_load_dwordx2 v[162:163], v[152:153], off offset:1024
	s_nop 0
	global_load_dwordx2 v[152:153], v[152:153], off offset:1536
	s_sub_i32 s2, s8, s3
	s_ashr_i32 s3, s2, 31
	s_lshl_b64 s[2:3], s[2:3], 5
	s_add_u32 s10, s12, s2
	s_addc_u32 s4, s13, s3
	s_lshr_b32 s11, s16, 1
	v_or_b32_e32 v154, s10, v120
	v_or_b32_e32 v156, s10, v122
	v_or_b32_e32 v176, s10, v124
	v_or_b32_e32 v188, s10, v126
	v_mov_b32_e32 v155, s4
	v_mov_b32_e32 v157, s4
	v_mov_b32_e32 v177, s4
	v_mov_b32_e32 v189, s4
	s_and_b32 s0, s11, 0x1c0
	v_lshlrev_b64 v[190:191], 12, v[154:155]
	v_lshlrev_b64 v[160:161], 9, v[156:157]
	v_lshlrev_b64 v[192:193], 12, v[156:157]
	v_lshlrev_b64 v[194:195], 12, v[176:177]
	v_lshlrev_b64 v[156:157], 9, v[188:189]
	v_lshlrev_b64 v[188:189], 12, v[188:189]
	s_lshl_b32 s4, s0, 1
	v_lshl_add_u64 v[190:191], v[102:103], 0, v[190:191]
	v_lshl_add_u64 v[192:193], v[102:103], 0, v[192:193]
	v_lshl_add_u64 v[194:195], v[102:103], 0, v[194:195]
	v_lshl_add_u64 v[188:189], v[102:103], 0, v[188:189]
	v_lshl_add_u64 v[200:201], v[190:191], 0, s[4:5]
	v_lshl_add_u64 v[202:203], v[192:193], 0, s[4:5]
	v_lshl_add_u64 v[204:205], v[194:195], 0, s[4:5]
	v_lshl_add_u64 v[206:207], v[188:189], 0, s[4:5]
	v_lshlrev_b64 v[158:159], 9, v[154:155]
	v_lshlrev_b64 v[154:155], 9, v[176:177]
	v_or_b32_e32 v158, v158, v116
	v_add_u32_e32 v185, 0x1000, v181
	v_add_u32_e32 v186, 0x1400, v181
	v_or_b32_e32 v160, v160, v116
	v_or_b32_e32 v154, v154, v116
	v_or_b32_e32 v156, v156, v116
	v_or_b32_e32 v158, s0, v158
	v_or_b32_e32 v160, s0, v160
	v_or_b32_e32 v154, s0, v154
	v_or_b32_e32 v156, s0, v156
	v_or_b32_e32 v187, s0, v116
	v_readfirstlane_b32 s22, v98
	v_readfirstlane_b32 s23, v99
	v_readfirstlane_b32 s24, v100
	v_readfirstlane_b32 s25, v101
	v_lshlrev_b32_e32 v176, 2, v187
	v_lshlrev_b32_e32 v118, 1, v116
	s_add_i32 s8, s8, s94
	s_cmpk_lt_i32 s8, 0x1000
	s_waitcnt vmcnt(53)
	v_lshlrev_b32_e32 v188, 16, v150
	v_and_b32_e32 v189, 0xffff0000, v150
	v_lshlrev_b32_e32 v190, 16, v151
	v_and_b32_e32 v191, 0xffff0000, v151
	s_waitcnt vmcnt(52)
	v_lshlrev_b32_e32 v192, 16, v148
	v_and_b32_e32 v193, 0xffff0000, v148
	v_lshlrev_b32_e32 v194, 16, v149
	v_and_b32_e32 v195, 0xffff0000, v149
	s_waitcnt vmcnt(51)
	v_lshlrev_b32_e32 v148, 16, v146
	v_and_b32_e32 v149, 0xffff0000, v146
	v_lshlrev_b32_e32 v150, 16, v147
	s_waitcnt vmcnt(42)
	v_mfma_f32_16x16x32_bf16 v[188:191], v[46:49], v[62:65], v[188:191]
	v_and_b32_e32 v151, 0xffff0000, v147
	v_lshlrev_b32_e32 v196, 16, v144
	v_and_b32_e32 v197, 0xffff0000, v144
	s_waitcnt vmcnt(38)
	v_mfma_f32_16x16x32_bf16 v[192:195], v[46:49], v[58:61], v[192:195]
	v_lshlrev_b32_e32 v198, 16, v145
	v_and_b32_e32 v199, 0xffff0000, v145
	v_lshlrev_b32_e32 v144, 16, v142
	s_waitcnt vmcnt(34)
	v_mfma_f32_16x16x32_bf16 v[148:151], v[46:49], v[54:57], v[148:151]
	v_and_b32_e32 v145, 0xffff0000, v142
	v_lshlrev_b32_e32 v146, 16, v143
	v_and_b32_e32 v147, 0xffff0000, v143
	s_waitcnt vmcnt(30)
	v_mfma_f32_16x16x32_bf16 v[46:49], v[46:49], v[50:53], v[196:199]
	v_lshlrev_b32_e32 v142, 16, v139
	v_and_b32_e32 v143, 0xffff0000, v139
	v_and_b32_e32 v139, 0xffff0000, v136
	v_lshlrev_b32_e32 v196, 16, v140
	v_and_b32_e32 v197, 0xffff0000, v140
	v_lshlrev_b32_e32 v198, 16, v141
	v_and_b32_e32 v199, 0xffff0000, v141
	v_lshlrev_b32_e32 v140, 16, v138
	v_and_b32_e32 v141, 0xffff0000, v138
	v_mfma_f32_16x16x32_bf16 v[58:61], v[42:45], v[58:61], v[196:199]
	v_lshlrev_b32_e32 v138, 16, v136
	v_mfma_f32_16x16x32_bf16 v[62:65], v[42:45], v[62:65], v[144:147]
	v_mfma_f32_16x16x32_bf16 v[54:57], v[42:45], v[54:57], v[140:143]
	s_waitcnt vmcnt(23)
	s_nop 0
	v_and_b32_e32 v144, 0xffff0000, v169
	v_lshlrev_b32_e32 v145, 16, v169
	v_and_b32_e32 v146, 0xffff0000, v168
	v_lshlrev_b32_e32 v140, 16, v137
	v_and_b32_e32 v141, 0xffff0000, v137
	v_lshlrev_b32_e32 v147, 16, v168
	s_waitcnt vmcnt(6)
	v_and_b32_e32 v168, 0xffff0000, v175
	v_mfma_f32_16x16x32_bf16 v[42:45], v[42:45], v[50:53], v[138:141]
	v_lshlrev_b32_e32 v169, 16, v175
	s_waitcnt vmcnt(5)
	v_lshlrev_b32_e32 v175, 16, v173
	v_mfma_f32_16x16x32_bf16 v[50:53], v[18:21], v[38:41], v[188:191]
	v_mfma_f32_16x16x32_bf16 v[136:139], v[18:21], v[34:37], v[192:195]
	s_nop 1
	v_and_b32_e32 v188, 0xffff0000, v174
	v_lshlrev_b32_e32 v189, 16, v174
	v_and_b32_e32 v174, 0xffff0000, v173
	v_mfma_f32_16x16x32_bf16 v[140:143], v[18:21], v[30:33], v[148:151]
	s_waitcnt vmcnt(4)
	v_lshlrev_b32_e32 v173, 16, v170
	v_mfma_f32_16x16x32_bf16 v[18:21], v[18:21], v[26:29], v[46:49]
	v_and_b32_e32 v148, 0xffff0000, v172
	v_lshlrev_b32_e32 v149, 16, v172
	v_and_b32_e32 v150, 0xffff0000, v171
	v_mfma_f32_16x16x32_bf16 v[34:37], v[14:17], v[34:37], v[58:61]
	v_lshlrev_b32_e32 v151, 16, v171
	v_and_b32_e32 v172, 0xffff0000, v170
	v_pk_add_f32 v[46:47], v[140:141], v[174:175]
	v_mfma_f32_16x16x32_bf16 v[38:41], v[14:17], v[38:41], v[62:65]
	s_waitcnt vmcnt(2)
	v_and_b32_e32 v60, 0xffff0000, v165
	v_lshlrev_b32_e32 v61, 16, v165
	v_and_b32_e32 v58, 0xffff0000, v166
	v_mfma_f32_16x16x32_bf16 v[30:33], v[14:17], v[30:33], v[54:57]
	v_and_b32_e32 v62, 0xffff0000, v167
	v_lshlrev_b32_e32 v63, 16, v167
	v_lshlrev_b32_e32 v59, 16, v166
	v_mfma_f32_16x16x32_bf16 v[14:17], v[14:17], v[26:29], v[42:45]
	v_add_f32_e64 v26, v50, v144
	v_add_f32_e64 v27, v51, v145
	v_pk_add_f32 v[28:29], v[52:53], v[146:147]
	v_and_b32_e32 v54, 0xffff0000, v164
	v_pk_add_f32 v[42:43], v[136:137], v[168:169]
	v_pk_add_f32 v[44:45], v[138:139], v[188:189]
	v_lshlrev_b32_e32 v55, 16, v164
	v_mfma_f32_16x16x32_bf16 v[26:29], v[22:25], v[94:97], v[26:29]
	v_add_f32_e64 v48, v142, v148
	v_add_f32_e64 v49, v143, v149
	v_pk_add_f32 v[18:19], v[18:19], v[150:151]
	v_pk_add_f32 v[20:21], v[20:21], v[172:173]
	v_mfma_f32_16x16x32_bf16 v[42:45], v[22:25], v[90:93], v[42:45]
	v_add_f32_e64 v34, v34, v60
	v_add_f32_e64 v35, v35, v61
	v_pk_add_f32 v[36:37], v[36:37], v[54:55]
	s_waitcnt vmcnt(1)
	v_and_b32_e32 v56, 0xffff0000, v163
	v_lshlrev_b32_e32 v57, 16, v163
	v_and_b32_e32 v52, 0xffff0000, v162
	v_mfma_f32_16x16x32_bf16 v[48:51], v[22:25], v[86:89], v[46:49]
	v_lshlrev_b32_e32 v53, 16, v162
	v_pk_add_f32 v[30:31], v[30:31], v[56:57]
	v_pk_add_f32 v[32:33], v[32:33], v[52:53]
	v_mfma_f32_16x16x32_bf16 v[18:21], v[22:25], v[82:85], v[18:21]
	s_waitcnt vmcnt(0)
	v_and_b32_e32 v46, 0xffff0000, v153
	v_pk_add_f32 v[22:23], v[38:39], v[62:63]
	v_pk_add_f32 v[24:25], v[40:41], v[58:59]
	v_lshlrev_b32_e32 v47, 16, v153
	v_mfma_f32_16x16x32_bf16 v[38:41], v[10:13], v[90:93], v[34:37]
	v_add_f32_e64 v14, v14, v46
	v_add_f32_e64 v15, v15, v47
	v_lshlrev_b64 v[52:53], 1, v[158:159]
	v_lshlrev_b64 v[54:55], 1, v[160:161]
	v_and_b32_e32 v34, 0xffff0000, v152
	v_lshlrev_b32_e32 v35, 16, v152
	v_pk_add_f32 v[16:17], v[16:17], v[34:35]
	v_mfma_f32_16x16x32_bf16 v[22:25], v[10:13], v[94:97], v[22:25]
	v_lshl_add_u64 v[90:91], v[104:105], 0, v[52:53]
	v_lshl_add_u64 v[92:93], v[106:107], 0, v[52:53]
	v_lshl_add_u64 v[94:95], v[108:109], 0, v[52:53]
	v_mfma_f32_16x16x32_bf16 v[30:33], v[10:13], v[86:89], v[30:33]
	v_lshlrev_b64 v[86:87], 1, v[154:155]
	v_lshlrev_b64 v[88:89], 1, v[156:157]
	v_lshl_add_u64 v[96:97], v[110:111], 0, v[52:53]
	v_mfma_f32_16x16x32_bf16 v[10:13], v[10:13], v[82:85], v[14:17]
	v_lshl_add_u64 v[58:59], v[104:105], 0, v[54:55]
	v_lshl_add_u64 v[60:61], v[106:107], 0, v[54:55]
	v_lshl_add_u64 v[62:63], v[108:109], 0, v[54:55]
	v_mfma_f32_16x16x32_bf16 v[14:17], v[6:9], v[78:81], v[26:29]
	v_lshl_add_u64 v[64:65], v[110:111], 0, v[54:55]
	v_lshl_add_u64 v[52:53], v[108:109], 0, v[86:87]
	v_lshl_add_u64 v[54:55], v[110:111], 0, v[86:87]
	v_mfma_f32_16x16x32_bf16 v[26:29], v[6:9], v[74:77], v[42:45]
	v_lshl_add_u64 v[56:57], v[200:201], 0, v[118:119]
	v_lshl_add_u64 v[46:47], v[202:203], 0, v[118:119]
	v_lshl_add_u64 v[36:37], v[204:205], 0, v[118:119]
	v_mfma_f32_16x16x32_bf16 v[82:85], v[6:9], v[70:73], v[48:51]
	v_lshl_add_u64 v[42:43], v[106:107], 0, v[88:89]
	v_lshl_add_u64 v[44:45], v[108:109], 0, v[88:89]
	v_lshl_add_u64 v[34:35], v[206:207], 0, v[118:119]
	v_mfma_f32_16x16x32_bf16 v[6:9], v[6:9], v[66:69], v[18:21]
	v_lshl_add_u64 v[48:49], v[104:105], 0, v[86:87]
	v_lshl_add_u64 v[50:51], v[106:107], 0, v[86:87]
	v_mfma_f32_16x16x32_bf16 v[18:21], v[2:5], v[78:81], v[22:25]
	v_mfma_f32_16x16x32_bf16 v[22:25], v[2:5], v[74:77], v[38:41]
	v_mfma_f32_16x16x32_bf16 v[30:33], v[2:5], v[70:73], v[30:33]
	s_nop 1
	v_lshl_add_u64 v[40:41], v[104:105], 0, v[88:89]
	v_lshl_add_u64 v[38:39], v[110:111], 0, v[88:89]
	v_mfma_f32_16x16x32_bf16 v[2:5], v[2:5], v[66:69], v[10:13]
	ds_write2_b32 v181, v14, v26 offset1:16
	ds_write2_b32 v181, v15, v27 offset0:68 offset1:84
	ds_write2_b32 v181, v16, v28 offset0:136 offset1:152
	ds_write2_b32 v181, v17, v29 offset0:204 offset1:220
	ds_write2_b32 v181, v82, v6 offset0:32 offset1:48
	ds_write2_b32 v181, v83, v7 offset0:100 offset1:116
	ds_write2_b32 v181, v84, v8 offset0:168 offset1:184
	ds_write2_b32 v181, v85, v9 offset0:236 offset1:252
	ds_write2_b32 v185, v18, v22 offset0:64 offset1:80
	ds_write2_b32 v185, v19, v23 offset0:132 offset1:148
	ds_write2_b32 v185, v20, v24 offset0:200 offset1:216
	ds_write2_b32 v186, v21, v25 offset0:12 offset1:28
	ds_write2_b32 v185, v30, v2 offset0:96 offset1:112
	ds_write2_b32 v185, v31, v3 offset0:164 offset1:180
	ds_write2_b32 v185, v32, v4 offset0:232 offset1:248
	ds_write2_b32 v186, v33, v5 offset0:44 offset1:60
	s_waitcnt lgkmcnt(0)
	ds_read_b128 v[66:69], v182
	ds_read_b128 v[70:73], v182 offset:16
	global_load_dwordx4 v[30:33], v[90:91], off
	global_load_dwordx4 v[26:29], v[92:93], off
	global_load_dwordx4 v[22:25], v[94:95], off
	global_load_dwordx4 v[18:21], v[96:97], off
	global_load_dwordx4 v[10:13], v176, s[22:23] offset:16
	global_load_dwordx4 v[14:17], v176, s[22:23]
	global_load_dwordx4 v[2:5], v176, s[24:25] offset:16
	global_load_dwordx4 v[6:9], v176, s[24:25]
	global_load_dwordx4 v[208:211], v[58:59], off
	global_load_dwordx4 v[212:215], v[60:61], off
	global_load_dwordx4 v[216:219], v[62:63], off
	global_load_dwordx4 v[220:223], v[64:65], off
	ds_read_b128 v[74:77], v182 offset:2176
	ds_read_b128 v[78:81], v182 offset:2192
	ds_read_b128 v[82:85], v182 offset:4352
	ds_read_b128 v[86:89], v182 offset:4368
	ds_read_b128 v[90:93], v182 offset:6528
	ds_read_b128 v[94:97], v182 offset:6544
	s_waitcnt lgkmcnt(5)
	v_add_f32_e32 v136, 0, v74
	v_add_f32_e32 v118, 0, v66
	s_waitcnt lgkmcnt(3)
	v_add_f32_e32 v137, 0, v82
	s_waitcnt lgkmcnt(1)
	v_add_f32_e32 v138, 0, v90
	v_add_f32_e32 v118, v67, v118
	v_add_f32_e32 v136, v75, v136
	v_add_f32_e32 v137, v83, v137
	v_add_f32_e32 v138, v91, v138
	v_add_f32_e32 v118, v68, v118
	v_add_f32_e32 v136, v76, v136
	v_add_f32_e32 v137, v84, v137
	v_add_f32_e32 v138, v92, v138
	v_add_f32_e32 v118, v69, v118
	v_add_f32_e32 v136, v77, v136
	v_add_f32_e32 v137, v85, v137
	v_add_f32_e32 v138, v93, v138
	v_add_f32_e32 v118, v70, v118
	v_add_f32_e32 v136, v78, v136
	v_add_f32_e32 v137, v86, v137
	s_waitcnt lgkmcnt(0)
	v_add_f32_e32 v138, v94, v138
	v_add_f32_e32 v118, v71, v118
	v_add_f32_e32 v136, v79, v136
	v_add_f32_e32 v137, v87, v137
	v_add_f32_e32 v138, v95, v138
	v_add_f32_e32 v118, v72, v118
	v_add_f32_e32 v136, v80, v136
	v_add_f32_e32 v137, v88, v137
	v_add_f32_e32 v138, v96, v138
	v_add_f32_e32 v118, v73, v118
	v_add_f32_e32 v136, v81, v136
	v_add_f32_e32 v137, v89, v137
	v_add_f32_e32 v138, v97, v138
	ds_bpermute_b32 v139, v1, v118
	ds_bpermute_b32 v140, v1, v136
	ds_bpermute_b32 v141, v1, v137
	ds_bpermute_b32 v142, v1, v138
	s_waitcnt lgkmcnt(3)
	v_add_f32_e32 v118, v118, v139
	s_waitcnt lgkmcnt(2)
	v_add_f32_e32 v136, v136, v140
	s_waitcnt lgkmcnt(1)
	v_add_f32_e32 v137, v137, v141
	s_waitcnt lgkmcnt(0)
	v_add_f32_e32 v138, v138, v142
	ds_bpermute_b32 v139, v117, v118
	ds_bpermute_b32 v140, v117, v136
	ds_bpermute_b32 v141, v117, v137
	ds_bpermute_b32 v142, v117, v138
	s_waitcnt lgkmcnt(3)
	v_add_f32_e32 v118, v118, v139
	s_waitcnt lgkmcnt(2)
	v_add_f32_e32 v136, v136, v140
	s_waitcnt lgkmcnt(1)
	v_add_f32_e32 v137, v137, v141
	s_waitcnt lgkmcnt(0)
	v_add_f32_e32 v138, v138, v142
	ds_bpermute_b32 v139, v121, v118
	ds_bpermute_b32 v140, v121, v136
	ds_bpermute_b32 v141, v121, v137
	ds_bpermute_b32 v142, v121, v138
	s_waitcnt lgkmcnt(3)
	v_add_f32_e32 v118, v118, v139
	s_waitcnt lgkmcnt(2)
	v_add_f32_e32 v136, v136, v140
	s_waitcnt lgkmcnt(1)
	v_add_f32_e32 v137, v137, v141
	s_waitcnt lgkmcnt(0)
	v_add_f32_e32 v139, v138, v142
	v_mul_f32_e32 v118, 0x3c800000, v118
	v_mul_f32_e32 v136, 0x3c800000, v136
	v_mul_f32_e32 v138, 0x3c800000, v137
	v_mul_f32_e32 v140, 0x3c800000, v139
	v_pk_add_f32 v[66:67], v[66:67], v[118:119] op_sel_hi:[1,0] neg_lo:[0,1] neg_hi:[0,1]
	v_pk_add_f32 v[68:69], v[68:69], v[118:119] op_sel_hi:[1,0] neg_lo:[0,1] neg_hi:[0,1]
	v_pk_add_f32 v[74:75], v[74:75], v[136:137] op_sel_hi:[1,0] neg_lo:[0,1] neg_hi:[0,1]
	v_pk_add_f32 v[82:83], v[82:83], v[138:139] op_sel_hi:[1,0] neg_lo:[0,1] neg_hi:[0,1]
	v_pk_add_f32 v[90:91], v[90:91], v[140:141] op_sel_hi:[1,0] neg_lo:[0,1] neg_hi:[0,1]
	v_pk_mul_f32 v[142:143], v[66:67], v[66:67]
	v_pk_add_f32 v[72:73], v[72:73], v[118:119] op_sel_hi:[1,0] neg_lo:[0,1] neg_hi:[0,1]
	v_pk_add_f32 v[70:71], v[70:71], v[118:119] op_sel_hi:[1,0] neg_lo:[0,1] neg_hi:[0,1]
	v_pk_add_f32 v[76:77], v[76:77], v[136:137] op_sel_hi:[1,0] neg_lo:[0,1] neg_hi:[0,1]
	v_pk_add_f32 v[84:85], v[84:85], v[138:139] op_sel_hi:[1,0] neg_lo:[0,1] neg_hi:[0,1]
	v_pk_add_f32 v[96:97], v[96:97], v[140:141] op_sel_hi:[1,0] neg_lo:[0,1] neg_hi:[0,1]
	v_pk_add_f32 v[94:95], v[94:95], v[140:141] op_sel_hi:[1,0] neg_lo:[0,1] neg_hi:[0,1]
	v_pk_add_f32 v[92:93], v[92:93], v[140:141] op_sel_hi:[1,0] neg_lo:[0,1] neg_hi:[0,1]
	v_pk_mul_f32 v[140:141], v[68:69], v[68:69]
	v_pk_mul_f32 v[150:151], v[74:75], v[74:75]
	v_pk_mul_f32 v[158:159], v[82:83], v[82:83]
	v_pk_mul_f32 v[166:167], v[90:91], v[90:91]
	v_add_f32_e32 v118, v142, v143
	v_pk_mul_f32 v[148:149], v[76:77], v[76:77]
	v_pk_mul_f32 v[156:157], v[84:85], v[84:85]
	v_pk_mul_f32 v[164:165], v[92:93], v[92:93]
	v_add_f32_e32 v142, v150, v151
	v_add_f32_e32 v143, v158, v159
	v_add_f32_e32 v150, v166, v167
	v_add_f32_e32 v118, v140, v118
	v_pk_add_f32 v[78:79], v[78:79], v[136:137] op_sel_hi:[1,0] neg_lo:[0,1] neg_hi:[0,1]
	v_pk_add_f32 v[88:89], v[88:89], v[138:139] op_sel_hi:[1,0] neg_lo:[0,1] neg_hi:[0,1]
	v_pk_add_f32 v[86:87], v[86:87], v[138:139] op_sel_hi:[1,0] neg_lo:[0,1] neg_hi:[0,1]
	v_pk_mul_f32 v[138:139], v[70:71], v[70:71]
	v_add_f32_e32 v140, v148, v142
	v_add_f32_e32 v142, v156, v143
	v_add_f32_e32 v143, v164, v150
	v_add_f32_e32 v118, v141, v118
	v_pk_mul_f32 v[146:147], v[78:79], v[78:79]
	v_pk_mul_f32 v[154:155], v[86:87], v[86:87]
	v_pk_mul_f32 v[162:163], v[94:95], v[94:95]
	v_add_f32_e32 v140, v149, v140
	v_add_f32_e32 v141, v157, v142
	v_add_f32_e32 v142, v165, v143
	v_add_f32_e32 v118, v138, v118
	v_pk_add_f32 v[80:81], v[80:81], v[136:137] op_sel_hi:[1,0] neg_lo:[0,1] neg_hi:[0,1]
	v_pk_mul_f32 v[136:137], v[72:73], v[72:73]
	v_add_f32_e32 v138, v146, v140
	v_add_f32_e32 v140, v154, v141
	v_add_f32_e32 v141, v162, v142
	v_add_f32_e32 v118, v139, v118
	v_pk_mul_f32 v[144:145], v[80:81], v[80:81]
	v_pk_mul_f32 v[152:153], v[88:89], v[88:89]
	v_pk_mul_f32 v[160:161], v[96:97], v[96:97]
	v_add_f32_e32 v138, v147, v138
	v_add_f32_e32 v139, v155, v140
	v_add_f32_e32 v140, v163, v141
	v_add_f32_e32 v118, v136, v118
	v_add_f32_e32 v136, v144, v138
	v_add_f32_e32 v138, v152, v139
	v_add_f32_e32 v139, v160, v140
	v_add_f32_e32 v118, v137, v118
	v_add_f32_e32 v136, v145, v136
	v_add_f32_e32 v137, v153, v138
	v_add_f32_e32 v138, v161, v139
	ds_bpermute_b32 v139, v1, v118
	ds_bpermute_b32 v140, v1, v136
	ds_bpermute_b32 v141, v1, v137
	ds_bpermute_b32 v142, v1, v138
	s_waitcnt lgkmcnt(3)
	v_add_f32_e32 v118, v118, v139
	s_waitcnt lgkmcnt(2)
	v_add_f32_e32 v136, v136, v140
	s_waitcnt lgkmcnt(1)
	v_add_f32_e32 v137, v137, v141
	s_waitcnt lgkmcnt(0)
	v_add_f32_e32 v138, v138, v142
	ds_bpermute_b32 v139, v117, v118
	ds_bpermute_b32 v140, v117, v136
	ds_bpermute_b32 v141, v117, v137
	ds_bpermute_b32 v142, v117, v138
	s_waitcnt lgkmcnt(3)
	v_add_f32_e32 v118, v118, v139
	s_waitcnt lgkmcnt(2)
	v_add_f32_e32 v136, v136, v140
	s_waitcnt lgkmcnt(1)
	v_add_f32_e32 v137, v137, v141
	s_waitcnt lgkmcnt(0)
	v_add_f32_e32 v138, v138, v142
	ds_bpermute_b32 v139, v121, v118
	ds_bpermute_b32 v140, v121, v136
	ds_bpermute_b32 v141, v121, v137
	ds_bpermute_b32 v142, v121, v138
	s_waitcnt lgkmcnt(3)
	v_add_f32_e32 v118, v118, v139
	s_waitcnt lgkmcnt(2)
	v_add_f32_e32 v136, v136, v140
	s_waitcnt lgkmcnt(1)
	v_add_f32_e32 v137, v137, v141
	s_waitcnt lgkmcnt(0)
	v_add_f32_e32 v138, v138, v142
	v_fmamk_f32 v118, v118, 0x3c800000, v183
	v_fmamk_f32 v136, v136, 0x3c800000, v183
	v_fmamk_f32 v137, v137, 0x3c800000, v183
	v_fmamk_f32 v138, v138, 0x3c800000, v183
	v_mul_f32_e32 v139, 0x4f800000, v118
	v_cmp_gt_f32_e64 s[12:13], s9, v118
	v_mul_f32_e32 v140, 0x4f800000, v136
	v_cmp_gt_f32_e32 vcc, s9, v136
	v_mul_f32_e32 v141, 0x4f800000, v137
	v_cmp_gt_f32_e64 s[0:1], s9, v137
	v_mul_f32_e32 v142, 0x4f800000, v138
	v_cmp_gt_f32_e64 s[6:7], s9, v138
	v_cndmask_b32_e64 v118, v118, v139, s[12:13]
	v_cndmask_b32_e32 v136, v136, v140, vcc
	v_cndmask_b32_e64 v137, v137, v141, s[0:1]
	v_cndmask_b32_e64 v138, v138, v142, s[6:7]
	v_sqrt_f32_e32 v139, v118
	v_sqrt_f32_e32 v140, v136
	v_sqrt_f32_e32 v141, v137
	v_sqrt_f32_e32 v142, v138
	v_add_u32_e32 v143, -1, v139
	v_add_u32_e32 v145, -1, v140
	v_add_u32_e32 v147, -1, v141
	v_add_u32_e32 v149, -1, v142
	v_fma_f32 v151, -v143, v139, v118
	v_add_u32_e32 v144, 1, v139
	v_add_u32_e32 v146, 1, v140
	v_add_u32_e32 v148, 1, v141
	v_add_u32_e32 v150, 1, v142
	v_fma_f32 v153, -v145, v140, v136
	v_fma_f32 v155, -v147, v141, v137
	v_fma_f32 v157, -v149, v142, v138
	v_cmp_ge_f32_e64 s[14:15], 0, v151
	v_fma_f32 v152, -v144, v139, v118
	v_fma_f32 v154, -v146, v140, v136
	v_fma_f32 v156, -v148, v141, v137
	v_fma_f32 v158, -v150, v142, v138
	v_cndmask_b32_e64 v139, v139, v143, s[14:15]
	v_cmp_ge_f32_e64 s[14:15], 0, v153
	v_cmp_ge_f32_e64 s[16:17], 0, v155
	v_cmp_ge_f32_e64 s[18:19], 0, v157
	v_cndmask_b32_e64 v140, v140, v145, s[14:15]
	v_cmp_lt_f32_e64 s[14:15], 0, v154
	v_cndmask_b32_e64 v141, v141, v147, s[16:17]
	v_cmp_lt_f32_e64 s[16:17], 0, v156
	v_cndmask_b32_e64 v142, v142, v149, s[18:19]
	v_cmp_lt_f32_e64 s[18:19], 0, v158
	v_cmp_lt_f32_e64 s[20:21], 0, v152
	v_cndmask_b32_e64 v140, v140, v146, s[14:15]
	v_cndmask_b32_e64 v141, v141, v148, s[16:17]
	v_cndmask_b32_e64 v139, v139, v144, s[20:21]
	v_cndmask_b32_e64 v142, v142, v150, s[18:19]
	v_mul_f32_e32 v143, 0x37800000, v139
	v_mul_f32_e32 v144, 0x37800000, v140
	v_mul_f32_e32 v145, 0x37800000, v141
	v_mul_f32_e32 v146, 0x37800000, v142
	v_cndmask_b32_e64 v139, v139, v143, s[12:13]
	v_cndmask_b32_e32 v140, v140, v144, vcc
	v_cmp_class_f32_e32 vcc, v136, v184
	v_cndmask_b32_e64 v141, v141, v145, s[0:1]
	v_cmp_class_f32_e64 s[0:1], v137, v184
	v_cndmask_b32_e64 v142, v142, v146, s[6:7]
	v_cmp_class_f32_e64 s[6:7], v138, v184
	v_cmp_class_f32_e64 s[12:13], v118, v184
	v_cndmask_b32_e32 v154, v140, v136, vcc
	v_cndmask_b32_e64 v155, v141, v137, s[0:1]
	v_cndmask_b32_e64 v118, v139, v118, s[12:13]
	v_cndmask_b32_e64 v156, v142, v138, s[6:7]
	v_div_scale_f32 v157, s[0:1], v118, v118, 1.0
	v_div_scale_f32 v159, s[0:1], v154, v154, 1.0
	v_div_scale_f32 v161, s[2:3], v155, v155, 1.0
	v_div_scale_f32 v163, s[2:3], v156, v156, 1.0
	v_rcp_f32_e32 v165, v157
	v_rcp_f32_e32 v166, v159
	v_rcp_f32_e32 v167, v161
	v_rcp_f32_e32 v168, v163
	v_fma_f32 v136, -v157, v165, 1.0
	v_fma_f32 v137, -v159, v166, 1.0
	v_fma_f32 v138, -v161, v167, 1.0
	v_fma_f32 v139, -v163, v168, 1.0
	v_div_scale_f32 v158, vcc, 1.0, v118, 1.0
	v_fmac_f32_e32 v165, v136, v165
	v_fmac_f32_e32 v166, v137, v166
	v_fmac_f32_e32 v167, v138, v167
	v_fmac_f32_e32 v168, v139, v168
	s_waitcnt vmcnt(11)
	v_and_b32_e32 v137, 0xffff0000, v30
	v_lshlrev_b32_e32 v136, 16, v30
	s_waitcnt vmcnt(10)
	v_and_b32_e32 v139, 0xffff0000, v26
	v_lshlrev_b32_e32 v138, 16, v26
	v_div_scale_f32 v160, s[0:1], 1.0, v154, 1.0
	v_and_b32_e32 v141, 0xffff0000, v31
	v_lshlrev_b32_e32 v140, 16, v31
	v_and_b32_e32 v31, 0xffff0000, v27
	v_lshlrev_b32_e32 v30, 16, v27
	v_and_b32_e32 v27, 0xffff0000, v32
	v_lshlrev_b32_e32 v26, 16, v32
	v_and_b32_e32 v143, 0xffff0000, v28
	v_lshlrev_b32_e32 v142, 16, v28
	v_and_b32_e32 v145, 0xffff0000, v33
	v_lshlrev_b32_e32 v144, 16, v33
	v_and_b32_e32 v33, 0xffff0000, v29
	v_lshlrev_b32_e32 v32, 16, v29
	s_waitcnt vmcnt(9)
	v_lshlrev_b32_e32 v28, 16, v25
	v_and_b32_e32 v29, 0xffff0000, v25
	s_waitcnt vmcnt(8)
	v_lshlrev_b32_e32 v146, 16, v21
	v_and_b32_e32 v147, 0xffff0000, v21
	v_lshlrev_b32_e32 v148, 16, v24
	v_and_b32_e32 v149, 0xffff0000, v24
	v_lshlrev_b32_e32 v24, 16, v20
	v_and_b32_e32 v25, 0xffff0000, v20
	v_lshlrev_b32_e32 v20, 16, v23
	v_and_b32_e32 v21, 0xffff0000, v23
	v_lshlrev_b32_e32 v150, 16, v19
	v_and_b32_e32 v151, 0xffff0000, v19
	v_lshlrev_b32_e32 v152, 16, v22
	v_and_b32_e32 v153, 0xffff0000, v22
	v_lshlrev_b32_e32 v22, 16, v18
	v_and_b32_e32 v23, 0xffff0000, v18
	v_mul_f32_e32 v169, v158, v165
	v_pk_mul_f32 v[18:19], v[136:137], v[138:139]
	v_div_scale_f32 v162, s[6:7], 1.0, v155, 1.0
	v_mul_f32_e32 v170, v160, v166
	v_fma_f32 v136, -v157, v169, v158
	s_waitcnt vmcnt(6)
	v_pk_mul_f32 v[14:15], v[18:19], v[14:15]
	v_div_scale_f32 v164, s[12:13], 1.0, v156, 1.0
	v_mul_f32_e32 v171, v162, v167
	v_pk_mul_f32 v[30:31], v[140:141], v[30:31]
	v_fma_f32 v137, -v159, v170, v160
	v_fmac_f32_e32 v169, v136, v165
	v_add_f32_e32 v14, 0, v14
	v_mul_f32_e32 v172, v164, v168
	v_fma_f32 v138, -v161, v171, v162
	v_pk_mul_f32 v[16:17], v[30:31], v[16:17]
	v_fmac_f32_e32 v170, v137, v166
	v_fma_f32 v18, -v157, v169, v158
	v_add_f32_e32 v14, v15, v14
	v_pk_mul_f32 v[26:27], v[26:27], v[142:143]
	v_pk_mul_f32 v[32:33], v[144:145], v[32:33]
	v_fma_f32 v139, -v163, v172, v164
	v_fmac_f32_e32 v171, v138, v167
	v_fma_f32 v19, -v159, v170, v160
	v_div_fmas_f32 v15, v18, v165, v169
	v_add_f32_e32 v16, v16, v14
	s_mov_b64 vcc, s[0:1]
	v_pk_mul_f32 v[10:11], v[26:27], v[10:11]
	v_pk_mul_f32 v[12:13], v[32:33], v[12:13]
	v_fmac_f32_e32 v172, v139, v168
	v_fma_f32 v31, -v161, v171, v162
	v_div_fixup_f32 v14, v15, v118, 1.0
	v_div_fmas_f32 v30, v19, v166, v170
	v_add_f32_e32 v33, v17, v16
	s_mov_b64 vcc, s[6:7]
	v_fma_f32 v32, -v163, v172, v164
	v_pk_mul_f32 v[16:17], v[66:67], v[14:15] op_sel_hi:[1,0]
	v_pk_mul_f32 v[18:19], v[68:69], v[14:15] op_sel_hi:[1,0]
	v_pk_mul_f32 v[26:27], v[70:71], v[14:15] op_sel_hi:[1,0]
	v_pk_mul_f32 v[14:15], v[72:73], v[14:15] op_sel_hi:[1,0]
	v_div_fmas_f32 v31, v31, v167, v171
	v_add_f32_e32 v33, v10, v33
	s_mov_b64 vcc, s[12:13]
	v_div_fixup_f32 v30, v30, v154, 1.0
	s_waitcnt vmcnt(5)
	v_pk_mul_f32 v[4:5], v[4:5], v[14:15]
	v_div_fixup_f32 v10, v31, v155, 1.0
	v_div_fmas_f32 v14, v32, v168, v172
	v_add_f32_e32 v11, v11, v33
	v_pk_mul_f32 v[66:67], v[74:75], v[30:31] op_sel_hi:[1,0]
	v_pk_mul_f32 v[68:69], v[76:77], v[30:31] op_sel_hi:[1,0]
	v_pk_mul_f32 v[70:71], v[78:79], v[30:31] op_sel_hi:[1,0]
	v_pk_mul_f32 v[72:73], v[80:81], v[30:31] op_sel_hi:[1,0]
	v_pk_mul_f32 v[74:75], v[82:83], v[10:11] op_sel_hi:[1,0]
	v_pk_mul_f32 v[76:77], v[84:85], v[10:11] op_sel_hi:[1,0]
	v_pk_mul_f32 v[78:79], v[86:87], v[10:11] op_sel_hi:[1,0]
	v_pk_mul_f32 v[80:81], v[88:89], v[10:11] op_sel_hi:[1,0]
	v_div_fixup_f32 v10, v14, v156, 1.0
	v_add_f32_e32 v11, v12, v11
	v_pk_mul_f32 v[82:83], v[90:91], v[10:11] op_sel_hi:[1,0]
	v_pk_mul_f32 v[84:85], v[92:93], v[10:11] op_sel_hi:[1,0]
	v_pk_mul_f32 v[86:87], v[94:95], v[10:11] op_sel_hi:[1,0]
	v_pk_mul_f32 v[88:89], v[96:97], v[10:11] op_sel_hi:[1,0]
	v_add_f32_e32 v10, v13, v11
	ds_bpermute_b32 v11, v1, v10
	s_waitcnt vmcnt(4)
	v_pk_mul_f32 v[6:7], v[6:7], v[16:17]
	v_pk_mul_f32 v[8:9], v[8:9], v[18:19]
	v_pk_mul_f32 v[2:3], v[2:3], v[26:27]
	s_waitcnt lgkmcnt(0)
	v_add_f32_e32 v10, v10, v11
	ds_bpermute_b32 v11, v117, v10
	s_waitcnt lgkmcnt(0)
	v_add_f32_e32 v10, v10, v11
	ds_bpermute_b32 v11, v121, v10
	s_waitcnt lgkmcnt(0)
	v_add_f32_e32 v10, v10, v11
	v_pk_fma_f32 v[6:7], v[10:11], v[152:153], v[6:7] op_sel_hi:[0,1,1]
	v_pk_fma_f32 v[8:9], v[10:11], v[20:21], v[8:9] op_sel_hi:[0,1,1]
	v_pk_fma_f32 v[2:3], v[10:11], v[148:149], v[2:3] op_sel_hi:[0,1,1]
	v_pk_fma_f32 v[4:5], v[10:11], v[28:29], v[4:5] op_sel_hi:[0,1,1]
	v_pk_mul_f32 v[6:7], v[6:7], v[22:23]
	v_pk_mul_f32 v[8:9], v[8:9], v[150:151]
	v_pk_mul_f32 v[10:11], v[2:3], v[24:25]
	v_pk_mul_f32 v[12:13], v[4:5], v[146:147]
	v_cvt_pk_bf16_f32 v2, v6, v7
	v_cvt_pk_bf16_f32 v3, v8, v9
	v_cvt_pk_bf16_f32 v4, v10, v11
	v_cvt_pk_bf16_f32 v5, v12, v13
	global_store_dwordx4 v[56:57], v[2:5], off offset:1024
	s_waitcnt vmcnt(1)
	s_nop 1
	v_mov_b64 v[2:3], v[208:209]
	v_mov_b64 v[4:5], v[210:211]
	s_nop 0
	v_mov_b64 v[6:7], v[212:213]
	v_mov_b64 v[8:9], v[214:215]
	v_mov_b64 v[10:11], v[216:217]
	v_mov_b64 v[12:13], v[218:219]
	v_mov_b64 v[14:15], v[220:221]
	v_mov_b64 v[16:17], v[222:223]
	global_load_dwordx4 v[18:21], v176, s[24:25]
	global_load_dwordx4 v[22:25], v176, s[24:25] offset:16
	global_load_dwordx4 v[26:29], v176, s[22:23]
	global_load_dwordx4 v[30:33], v176, s[22:23] offset:16
	global_load_dwordx4 v[208:211], v[48:49], off
	global_load_dwordx4 v[212:215], v[50:51], off
	global_load_dwordx4 v[216:219], v[52:53], off
	global_load_dwordx4 v[220:223], v[54:55], off
	v_and_b32_e32 v57, 0xffff0000, v2
	v_lshlrev_b32_e32 v56, 16, v2
	v_and_b32_e32 v59, 0xffff0000, v6
	v_lshlrev_b32_e32 v58, 16, v6
	v_and_b32_e32 v61, 0xffff0000, v3
	v_lshlrev_b32_e32 v60, 16, v3
	v_and_b32_e32 v3, 0xffff0000, v7
	v_lshlrev_b32_e32 v2, 16, v7
	v_and_b32_e32 v7, 0xffff0000, v4
	v_lshlrev_b32_e32 v6, 16, v4
	v_and_b32_e32 v63, 0xffff0000, v8
	v_lshlrev_b32_e32 v62, 16, v8
	v_and_b32_e32 v65, 0xffff0000, v5
	v_lshlrev_b32_e32 v64, 16, v5
	v_and_b32_e32 v5, 0xffff0000, v9
	v_lshlrev_b32_e32 v4, 16, v9
	v_lshlrev_b32_e32 v8, 16, v13
	v_and_b32_e32 v9, 0xffff0000, v13
	v_lshlrev_b32_e32 v90, 16, v17
	v_and_b32_e32 v91, 0xffff0000, v17
	v_lshlrev_b32_e32 v92, 16, v12
	v_and_b32_e32 v93, 0xffff0000, v12
	v_lshlrev_b32_e32 v12, 16, v16
	v_and_b32_e32 v13, 0xffff0000, v16
	v_lshlrev_b32_e32 v16, 16, v11
	v_and_b32_e32 v17, 0xffff0000, v11
	v_lshlrev_b32_e32 v94, 16, v15
	v_and_b32_e32 v95, 0xffff0000, v15
	v_lshlrev_b32_e32 v96, 16, v10
	v_and_b32_e32 v97, 0xffff0000, v10
	v_lshlrev_b32_e32 v10, 16, v14
	v_and_b32_e32 v11, 0xffff0000, v14
	s_waitcnt vmcnt(7)
	v_pk_mul_f32 v[14:15], v[18:19], v[66:67]
	v_pk_mul_f32 v[18:19], v[20:21], v[68:69]
	s_waitcnt vmcnt(6)
	v_pk_mul_f32 v[20:21], v[22:23], v[70:71]
	v_pk_mul_f32 v[22:23], v[24:25], v[72:73]
	v_pk_mul_f32 v[24:25], v[56:57], v[58:59]
	v_pk_mul_f32 v[2:3], v[60:61], v[2:3]
	s_waitcnt vmcnt(5)
	v_pk_mul_f32 v[24:25], v[24:25], v[26:27]
	v_pk_mul_f32 v[2:3], v[2:3], v[28:29]
	v_add_f32_e32 v24, 0, v24
	v_add_f32_e32 v24, v25, v24
	v_pk_mul_f32 v[6:7], v[6:7], v[62:63]
	v_add_f32_e32 v2, v2, v24
	s_waitcnt vmcnt(4)
	v_pk_mul_f32 v[6:7], v[6:7], v[30:31]
	v_add_f32_e32 v2, v3, v2
	v_pk_mul_f32 v[4:5], v[64:65], v[4:5]
	v_add_f32_e32 v2, v6, v2
	v_pk_mul_f32 v[4:5], v[4:5], v[32:33]
	v_add_f32_e32 v2, v7, v2
	v_add_f32_e32 v2, v4, v2
	v_add_f32_e32 v2, v5, v2
	ds_bpermute_b32 v3, v1, v2
	s_waitcnt lgkmcnt(0)
	v_add_f32_e32 v2, v2, v3
	ds_bpermute_b32 v3, v117, v2
	s_waitcnt lgkmcnt(0)
	v_add_f32_e32 v2, v2, v3
	ds_bpermute_b32 v3, v121, v2
	s_waitcnt lgkmcnt(0)
	v_add_f32_e32 v2, v2, v3
	v_pk_fma_f32 v[4:5], v[2:3], v[96:97], v[14:15] op_sel_hi:[0,1,1]
	v_pk_fma_f32 v[6:7], v[2:3], v[16:17], v[18:19] op_sel_hi:[0,1,1]
	v_pk_fma_f32 v[14:15], v[2:3], v[92:93], v[20:21] op_sel_hi:[0,1,1]
	v_pk_fma_f32 v[2:3], v[2:3], v[8:9], v[22:23] op_sel_hi:[0,1,1]
	v_pk_mul_f32 v[4:5], v[4:5], v[10:11]
	v_pk_mul_f32 v[6:7], v[6:7], v[94:95]
	v_pk_mul_f32 v[8:9], v[14:15], v[12:13]
	v_pk_mul_f32 v[10:11], v[2:3], v[90:91]
	v_cvt_pk_bf16_f32 v2, v4, v5
	v_cvt_pk_bf16_f32 v3, v6, v7
	v_cvt_pk_bf16_f32 v4, v8, v9
	v_cvt_pk_bf16_f32 v5, v10, v11
	global_store_dwordx4 v[46:47], v[2:5], off offset:1024
	s_waitcnt vmcnt(1)
	s_nop 1
	v_mov_b64 v[2:3], v[208:209]
	v_mov_b64 v[4:5], v[210:211]
	s_nop 0
	v_mov_b64 v[6:7], v[212:213]
	v_mov_b64 v[8:9], v[214:215]
	v_mov_b64 v[10:11], v[216:217]
	v_mov_b64 v[12:13], v[218:219]
	v_mov_b64 v[14:15], v[220:221]
	v_mov_b64 v[16:17], v[222:223]
	global_load_dwordx4 v[18:21], v176, s[24:25]
	global_load_dwordx4 v[22:25], v176, s[24:25] offset:16
	global_load_dwordx4 v[26:29], v176, s[22:23]
	global_load_dwordx4 v[30:33], v176, s[22:23] offset:16
	global_load_dwordx4 v[208:211], v[40:41], off
	global_load_dwordx4 v[212:215], v[42:43], off
	global_load_dwordx4 v[216:219], v[44:45], off
	global_load_dwordx4 v[220:223], v[38:39], off
	v_and_b32_e32 v47, 0xffff0000, v2
	v_lshlrev_b32_e32 v46, 16, v2
	v_and_b32_e32 v49, 0xffff0000, v6
	v_lshlrev_b32_e32 v48, 16, v6
	v_and_b32_e32 v51, 0xffff0000, v3
	v_lshlrev_b32_e32 v50, 16, v3
	v_and_b32_e32 v3, 0xffff0000, v7
	v_lshlrev_b32_e32 v2, 16, v7
	v_and_b32_e32 v7, 0xffff0000, v4
	v_lshlrev_b32_e32 v6, 16, v4
	v_and_b32_e32 v53, 0xffff0000, v8
	v_lshlrev_b32_e32 v52, 16, v8
	v_and_b32_e32 v55, 0xffff0000, v5
	v_lshlrev_b32_e32 v54, 16, v5
	v_and_b32_e32 v5, 0xffff0000, v9
	v_lshlrev_b32_e32 v4, 16, v9
	v_lshlrev_b32_e32 v8, 16, v13
	v_and_b32_e32 v9, 0xffff0000, v13
	v_lshlrev_b32_e32 v56, 16, v17
	v_and_b32_e32 v57, 0xffff0000, v17
	v_lshlrev_b32_e32 v58, 16, v12
	v_and_b32_e32 v59, 0xffff0000, v12
	v_lshlrev_b32_e32 v12, 16, v16
	v_and_b32_e32 v13, 0xffff0000, v16
	v_lshlrev_b32_e32 v16, 16, v11
	v_and_b32_e32 v17, 0xffff0000, v11
	v_lshlrev_b32_e32 v60, 16, v15
	v_and_b32_e32 v61, 0xffff0000, v15
	v_lshlrev_b32_e32 v62, 16, v10
	v_and_b32_e32 v63, 0xffff0000, v10
	v_lshlrev_b32_e32 v10, 16, v14
	v_and_b32_e32 v11, 0xffff0000, v14
	s_waitcnt vmcnt(7)
	v_pk_mul_f32 v[14:15], v[18:19], v[74:75]
	v_pk_mul_f32 v[18:19], v[20:21], v[76:77]
	s_waitcnt vmcnt(6)
	v_pk_mul_f32 v[20:21], v[22:23], v[78:79]
	v_pk_mul_f32 v[22:23], v[24:25], v[80:81]
	v_pk_mul_f32 v[24:25], v[46:47], v[48:49]
	v_pk_mul_f32 v[2:3], v[50:51], v[2:3]
	s_waitcnt vmcnt(5)
	v_pk_mul_f32 v[24:25], v[24:25], v[26:27]
	v_pk_mul_f32 v[2:3], v[2:3], v[28:29]
	v_add_f32_e32 v24, 0, v24
	v_add_f32_e32 v24, v25, v24
	v_pk_mul_f32 v[6:7], v[6:7], v[52:53]
	v_add_f32_e32 v2, v2, v24
	s_waitcnt vmcnt(4)
	v_pk_mul_f32 v[6:7], v[6:7], v[30:31]
	v_add_f32_e32 v2, v3, v2
	v_pk_mul_f32 v[4:5], v[54:55], v[4:5]
	v_add_f32_e32 v2, v6, v2
	v_pk_mul_f32 v[4:5], v[4:5], v[32:33]
	v_add_f32_e32 v2, v7, v2
	v_add_f32_e32 v2, v4, v2
	v_add_f32_e32 v2, v5, v2
	ds_bpermute_b32 v3, v1, v2
	s_waitcnt lgkmcnt(0)
	v_add_f32_e32 v2, v2, v3
	ds_bpermute_b32 v3, v117, v2
	s_waitcnt lgkmcnt(0)
	v_add_f32_e32 v2, v2, v3
	ds_bpermute_b32 v3, v121, v2
	s_waitcnt lgkmcnt(0)
	v_add_f32_e32 v2, v2, v3
	v_pk_fma_f32 v[4:5], v[2:3], v[62:63], v[14:15] op_sel_hi:[0,1,1]
	v_pk_fma_f32 v[6:7], v[2:3], v[16:17], v[18:19] op_sel_hi:[0,1,1]
	v_pk_fma_f32 v[14:15], v[2:3], v[58:59], v[20:21] op_sel_hi:[0,1,1]
	v_pk_fma_f32 v[2:3], v[2:3], v[8:9], v[22:23] op_sel_hi:[0,1,1]
	v_pk_mul_f32 v[4:5], v[4:5], v[10:11]
	v_pk_mul_f32 v[6:7], v[6:7], v[60:61]
	v_pk_mul_f32 v[8:9], v[14:15], v[12:13]
	v_pk_mul_f32 v[10:11], v[2:3], v[56:57]
	v_cvt_pk_bf16_f32 v2, v4, v5
	v_cvt_pk_bf16_f32 v3, v6, v7
	v_cvt_pk_bf16_f32 v4, v8, v9
	v_cvt_pk_bf16_f32 v5, v10, v11
	global_store_dwordx4 v[36:37], v[2:5], off offset:1024
	s_waitcnt vmcnt(1)
	s_nop 1
	v_mov_b64 v[2:3], v[208:209]
	v_mov_b64 v[4:5], v[210:211]
	s_nop 0
	v_mov_b64 v[6:7], v[212:213]
	v_mov_b64 v[8:9], v[214:215]
	v_mov_b64 v[10:11], v[216:217]
	v_mov_b64 v[12:13], v[218:219]
	global_load_dwordx4 v[14:17], v176, s[22:23] offset:16
	global_load_dwordx4 v[18:21], v176, s[22:23]
	global_load_dwordx4 v[22:25], v176, s[24:25] offset:16
	global_load_dwordx4 v[26:29], v176, s[24:25]
	v_mov_b64 v[30:31], v[220:221]
	v_mov_b64 v[32:33], v[222:223]
	v_and_b32_e32 v37, 0xffff0000, v2
	v_lshlrev_b32_e32 v36, 16, v2
	v_and_b32_e32 v39, 0xffff0000, v6
	v_lshlrev_b32_e32 v38, 16, v6
	v_and_b32_e32 v41, 0xffff0000, v3
	v_lshlrev_b32_e32 v40, 16, v3
	v_and_b32_e32 v3, 0xffff0000, v7
	v_lshlrev_b32_e32 v2, 16, v7
	v_and_b32_e32 v7, 0xffff0000, v4
	v_lshlrev_b32_e32 v6, 16, v4
	v_and_b32_e32 v43, 0xffff0000, v8
	v_lshlrev_b32_e32 v42, 16, v8
	v_and_b32_e32 v45, 0xffff0000, v5
	v_lshlrev_b32_e32 v44, 16, v5
	v_and_b32_e32 v5, 0xffff0000, v9
	v_lshlrev_b32_e32 v4, 16, v9
	v_lshlrev_b32_e32 v8, 16, v13
	v_and_b32_e32 v9, 0xffff0000, v13
	s_waitcnt vmcnt(0)
	v_lshlrev_b32_e32 v46, 16, v33
	v_and_b32_e32 v47, 0xffff0000, v33
	v_lshlrev_b32_e32 v48, 16, v12
	v_and_b32_e32 v49, 0xffff0000, v12
	v_lshlrev_b32_e32 v12, 16, v32
	v_and_b32_e32 v13, 0xffff0000, v32
	v_lshlrev_b32_e32 v32, 16, v11
	v_and_b32_e32 v33, 0xffff0000, v11
	v_lshlrev_b32_e32 v50, 16, v31
	v_and_b32_e32 v51, 0xffff0000, v31
	v_lshlrev_b32_e32 v52, 16, v10
	v_and_b32_e32 v53, 0xffff0000, v10
	v_lshlrev_b32_e32 v10, 16, v30
	v_and_b32_e32 v11, 0xffff0000, v30
	v_pk_mul_f32 v[30:31], v[36:37], v[38:39]
	v_pk_mul_f32 v[6:7], v[6:7], v[42:43]
	v_pk_mul_f32 v[18:19], v[30:31], v[18:19]
	v_pk_mul_f32 v[2:3], v[40:41], v[2:3]
	v_pk_mul_f32 v[6:7], v[6:7], v[14:15]
	v_add_f32_e32 v14, 0, v18
	v_pk_mul_f32 v[2:3], v[2:3], v[20:21]
	v_add_f32_e32 v14, v19, v14
	v_add_f32_e32 v2, v2, v14
	v_add_f32_e32 v2, v3, v2
	v_pk_mul_f32 v[4:5], v[44:45], v[4:5]
	v_add_f32_e32 v2, v6, v2
	v_pk_mul_f32 v[4:5], v[4:5], v[16:17]
	v_add_f32_e32 v2, v7, v2
	v_add_f32_e32 v2, v4, v2
	v_add_f32_e32 v2, v5, v2
	ds_bpermute_b32 v3, v1, v2
	v_pk_mul_f32 v[26:27], v[26:27], v[82:83]
	v_pk_mul_f32 v[28:29], v[28:29], v[84:85]
	v_pk_mul_f32 v[22:23], v[22:23], v[86:87]
	v_pk_mul_f32 v[24:25], v[24:25], v[88:89]
	s_waitcnt lgkmcnt(0)
	v_add_f32_e32 v2, v2, v3
	ds_bpermute_b32 v3, v117, v2
	s_waitcnt lgkmcnt(0)
	v_add_f32_e32 v2, v2, v3
	ds_bpermute_b32 v3, v121, v2
	s_waitcnt lgkmcnt(0)
	v_add_f32_e32 v2, v2, v3
	v_pk_fma_f32 v[4:5], v[2:3], v[52:53], v[26:27] op_sel_hi:[0,1,1]
	v_pk_fma_f32 v[6:7], v[2:3], v[32:33], v[28:29] op_sel_hi:[0,1,1]
	v_pk_fma_f32 v[14:15], v[2:3], v[48:49], v[22:23] op_sel_hi:[0,1,1]
	v_pk_fma_f32 v[2:3], v[2:3], v[8:9], v[24:25] op_sel_hi:[0,1,1]
	v_pk_mul_f32 v[4:5], v[4:5], v[10:11]
	v_pk_mul_f32 v[6:7], v[6:7], v[50:51]
	v_pk_mul_f32 v[8:9], v[14:15], v[12:13]
	v_pk_mul_f32 v[10:11], v[2:3], v[46:47]
	v_cvt_pk_bf16_f32 v2, v4, v5
	v_cvt_pk_bf16_f32 v3, v6, v7
	v_cvt_pk_bf16_f32 v4, v8, v9
	v_cvt_pk_bf16_f32 v5, v10, v11
	global_store_dwordx4 v[34:35], v[2:5], off offset:1024
	s_waitcnt lgkmcnt(0)
	s_cbranch_scc1 .LBB0_3735
